# speedup vs baseline: 1.0340x; 1.0007x over previous
.LBB0_50:
	s_andn2_b64 vcc, exec, s[4:5]
	s_cbranch_vccnz .LBB0_55
	v_lshrrev_b32_e32 v1, 6, v0
	v_lshl_or_b32 v1, s2, 2, v1
	s_movk_i32 s0, 0x271
	v_cmp_gt_u32_e32 vcc, s0, v1
	s_and_saveexec_b64 s[0:1], vcc
	s_cbranch_execz .LBB0_55
	v_mul_u32_u24_e32 v2, 0xa3e, v1
	v_lshrrev_b32_e32 v6, 16, v2
	v_mul_u32_u24_e32 v2, 25, v6
	v_and_b32_e32 v7, 15, v0
	v_sub_u32_e32 v8, v1, v2
	v_bfe_u32 v9, v0, 4, 2
	v_mov_b32_e32 v19, 0
	v_lshl_or_b32 v2, v6, 4, v7
	v_mul_u32_u24_e32 v1, 0x640, v2
	v_lshl_add_u32 v1, v9, 5, v1
	v_mul_u32_u24_e32 v2, 0x3200, v9
	v_lshl_add_u32 v2, v8, 6, v2
	v_lshl_add_u32 v2, v7, 2, v2
	s_waitcnt lgkmcnt(0)
	v_add_u32_e32 v4, 0x12c0, v2
	v_add_u32_e32 v5, 0x2580, v2
	global_load_dwordx4 v[36:39], v1, s[10:11]
	global_load_dwordx4 v[40:43], v1, s[10:11] offset:16
	global_load_dword v28, v2, s[10:11]
	global_load_dword v29, v2, s[10:11] offset:1600
	global_load_dword v30, v2, s[10:11] offset:3200
	global_load_dword v31, v4, s[10:11]
	global_load_dword v32, v4, s[10:11] offset:1600
	global_load_dword v33, v4, s[10:11] offset:3200
	global_load_dword v34, v5, s[10:11]
	global_load_dword v35, v5, s[10:11] offset:1600
	v_add_u32_e32 v3, 0xc800, v2
	v_add_u32_e32 v4, 0xdac0, v2
	v_add_u32_e32 v5, 0xed80, v2
	global_load_dwordx4 v[52:55], v1, s[10:11] offset:128
	global_load_dwordx4 v[56:59], v1, s[10:11] offset:144
	global_load_dword v44, v3, s[10:11]
	global_load_dword v45, v3, s[10:11] offset:1600
	global_load_dword v46, v3, s[10:11] offset:3200
	global_load_dword v47, v4, s[10:11]
	global_load_dword v48, v4, s[10:11] offset:1600
	global_load_dword v49, v4, s[10:11] offset:3200
	global_load_dword v50, v5, s[10:11]
	global_load_dword v51, v5, s[10:11] offset:1600
	v_add_u32_e32 v3, 0x19000, v2
	v_add_u32_e32 v4, 0x1a2c0, v2
	v_add_u32_e32 v5, 0x1b580, v2
	global_load_dwordx4 v[68:71], v1, s[10:11] offset:256
	global_load_dwordx4 v[72:75], v1, s[10:11] offset:272
	global_load_dword v60, v3, s[10:11]
	global_load_dword v61, v3, s[10:11] offset:1600
	global_load_dword v62, v3, s[10:11] offset:3200
	global_load_dword v63, v4, s[10:11]
	global_load_dword v64, v4, s[10:11] offset:1600
	global_load_dword v65, v4, s[10:11] offset:3200
	global_load_dword v66, v5, s[10:11]
	global_load_dword v67, v5, s[10:11] offset:1600
	v_add_u32_e32 v3, 0x25800, v2
	v_add_u32_e32 v4, 0x26ac0, v2
	v_add_u32_e32 v5, 0x27d80, v2
	global_load_dwordx4 v[84:87], v1, s[10:11] offset:384
	global_load_dwordx4 v[88:91], v1, s[10:11] offset:400
	global_load_dword v76, v3, s[10:11]
	global_load_dword v77, v3, s[10:11] offset:1600
	global_load_dword v78, v3, s[10:11] offset:3200
	global_load_dword v79, v4, s[10:11]
	global_load_dword v80, v4, s[10:11] offset:1600
	global_load_dword v81, v4, s[10:11] offset:3200
	global_load_dword v82, v5, s[10:11]
	global_load_dword v83, v5, s[10:11] offset:1600
	v_add_u32_e32 v3, 0x32000, v2
	v_add_u32_e32 v4, 0x332c0, v2
	v_add_u32_e32 v5, 0x34580, v2
	global_load_dwordx4 v[100:103], v1, s[10:11] offset:512
	global_load_dwordx4 v[104:107], v1, s[10:11] offset:528
	global_load_dword v92, v3, s[10:11]
	global_load_dword v93, v3, s[10:11] offset:1600
	global_load_dword v94, v3, s[10:11] offset:3200
	global_load_dword v95, v4, s[10:11]
	global_load_dword v96, v4, s[10:11] offset:1600
	global_load_dword v97, v4, s[10:11] offset:3200
	global_load_dword v98, v5, s[10:11]
	global_load_dword v99, v5, s[10:11] offset:1600
	v_add_u32_e32 v3, 0x3e800, v2
	v_add_u32_e32 v4, 0x3fac0, v2
	v_add_u32_e32 v5, 0x40d80, v2
	global_load_dwordx4 v[116:119], v1, s[10:11] offset:640
	global_load_dwordx4 v[120:123], v1, s[10:11] offset:656
	global_load_dword v108, v3, s[10:11]
	global_load_dword v109, v3, s[10:11] offset:1600
	global_load_dword v110, v3, s[10:11] offset:3200
	global_load_dword v111, v4, s[10:11]
	global_load_dword v112, v4, s[10:11] offset:1600
	global_load_dword v113, v4, s[10:11] offset:3200
	global_load_dword v114, v5, s[10:11]
	global_load_dword v115, v5, s[10:11] offset:1600
	s_waitcnt vmcnt(50)
	v_cvt_pk_f16_f32 v10, v28, v29
	v_cvt_pk_f16_f32 v11, v30, v31
	v_cvt_pk_f16_f32 v12, v32, v33
	v_cvt_pk_f16_f32 v13, v34, v35
	v_cvt_pk_f16_f32 v14, v36, v37
	v_cvt_pk_f16_f32 v15, v38, v39
	v_cvt_pk_f16_f32 v16, v40, v41
	v_cvt_pk_f16_f32 v17, v42, v43
	v_add_u32_e32 v3, 0x4b000, v2
	v_add_u32_e32 v4, 0x4c2c0, v2
	v_add_u32_e32 v5, 0x4d580, v2
	global_load_dwordx4 v[36:39], v1, s[10:11] offset:768
	global_load_dwordx4 v[40:43], v1, s[10:11] offset:784
	global_load_dword v28, v3, s[10:11]
	global_load_dword v29, v3, s[10:11] offset:1600
	global_load_dword v30, v3, s[10:11] offset:3200
	global_load_dword v31, v4, s[10:11]
	global_load_dword v32, v4, s[10:11] offset:1600
	global_load_dword v33, v4, s[10:11] offset:3200
	global_load_dword v34, v5, s[10:11]
	global_load_dword v35, v5, s[10:11] offset:1600
	s_nop 1
	v_mfma_f32_16x16x32_f16 a[0:3], v[10:13], v[14:17], 0
	s_waitcnt vmcnt(50)
	v_cvt_pk_f16_f32 v20, v44, v45
	v_cvt_pk_f16_f32 v21, v46, v47
	v_cvt_pk_f16_f32 v22, v48, v49
	v_cvt_pk_f16_f32 v23, v50, v51
	v_cvt_pk_f16_f32 v24, v52, v53
	v_cvt_pk_f16_f32 v25, v54, v55
	v_cvt_pk_f16_f32 v26, v56, v57
	v_cvt_pk_f16_f32 v27, v58, v59
	v_add_u32_e32 v3, 0x57800, v2
	v_add_u32_e32 v4, 0x58ac0, v2
	v_add_u32_e32 v5, 0x59d80, v2
	global_load_dwordx4 v[52:55], v1, s[10:11] offset:896
	global_load_dwordx4 v[56:59], v1, s[10:11] offset:912
	global_load_dword v44, v3, s[10:11]
	global_load_dword v45, v3, s[10:11] offset:1600
	global_load_dword v46, v3, s[10:11] offset:3200
	global_load_dword v47, v4, s[10:11]
	global_load_dword v48, v4, s[10:11] offset:1600
	global_load_dword v49, v4, s[10:11] offset:3200
	global_load_dword v50, v5, s[10:11]
	global_load_dword v51, v5, s[10:11] offset:1600
	s_nop 1
	v_mfma_f32_16x16x32_f16 a[0:3], v[20:23], v[24:27], a[0:3]
	s_waitcnt vmcnt(50)
	v_cvt_pk_f16_f32 v10, v60, v61
	v_cvt_pk_f16_f32 v11, v62, v63
	v_cvt_pk_f16_f32 v12, v64, v65
	v_cvt_pk_f16_f32 v13, v66, v67
	v_cvt_pk_f16_f32 v14, v68, v69
	v_cvt_pk_f16_f32 v15, v70, v71
	v_cvt_pk_f16_f32 v16, v72, v73
	v_cvt_pk_f16_f32 v17, v74, v75
	v_add_u32_e32 v3, 0x64000, v2
	v_add_u32_e32 v4, 0x652c0, v2
	v_add_u32_e32 v5, 0x66580, v2
	global_load_dwordx4 v[68:71], v1, s[10:11] offset:1024
	global_load_dwordx4 v[72:75], v1, s[10:11] offset:1040
	global_load_dword v60, v3, s[10:11]
	global_load_dword v61, v3, s[10:11] offset:1600
	global_load_dword v62, v3, s[10:11] offset:3200
	global_load_dword v63, v4, s[10:11]
	global_load_dword v64, v4, s[10:11] offset:1600
	global_load_dword v65, v4, s[10:11] offset:3200
	global_load_dword v66, v5, s[10:11]
	global_load_dword v67, v5, s[10:11] offset:1600
	s_nop 1
	v_mfma_f32_16x16x32_f16 a[0:3], v[10:13], v[14:17], a[0:3]
	s_waitcnt vmcnt(50)
	v_cvt_pk_f16_f32 v20, v76, v77
	v_cvt_pk_f16_f32 v21, v78, v79
	v_cvt_pk_f16_f32 v22, v80, v81
	v_cvt_pk_f16_f32 v23, v82, v83
	v_cvt_pk_f16_f32 v24, v84, v85
	v_cvt_pk_f16_f32 v25, v86, v87
	v_cvt_pk_f16_f32 v26, v88, v89
	v_cvt_pk_f16_f32 v27, v90, v91
	v_add_u32_e32 v3, 0x70800, v2
	v_add_u32_e32 v4, 0x71ac0, v2
	v_add_u32_e32 v5, 0x72d80, v2
	global_load_dwordx4 v[84:87], v1, s[10:11] offset:1152
	global_load_dwordx4 v[88:91], v1, s[10:11] offset:1168
	global_load_dword v76, v3, s[10:11]
	global_load_dword v77, v3, s[10:11] offset:1600
	global_load_dword v78, v3, s[10:11] offset:3200
	global_load_dword v79, v4, s[10:11]
	global_load_dword v80, v4, s[10:11] offset:1600
	global_load_dword v81, v4, s[10:11] offset:3200
	global_load_dword v82, v5, s[10:11]
	global_load_dword v83, v5, s[10:11] offset:1600
	s_nop 1
	v_mfma_f32_16x16x32_f16 a[0:3], v[20:23], v[24:27], a[0:3]
	s_waitcnt vmcnt(50)
	v_cvt_pk_f16_f32 v10, v92, v93
	v_cvt_pk_f16_f32 v11, v94, v95
	v_cvt_pk_f16_f32 v12, v96, v97
	v_cvt_pk_f16_f32 v13, v98, v99
	v_cvt_pk_f16_f32 v14, v100, v101
	v_cvt_pk_f16_f32 v15, v102, v103
	v_cvt_pk_f16_f32 v16, v104, v105
	v_cvt_pk_f16_f32 v17, v106, v107
	v_add_u32_e32 v3, 0x7d000, v2
	v_add_u32_e32 v4, 0x7e2c0, v2
	v_add_u32_e32 v5, 0x7f580, v2
	global_load_dwordx4 v[100:103], v1, s[10:11] offset:1280
	global_load_dwordx4 v[104:107], v1, s[10:11] offset:1296
	global_load_dword v92, v3, s[10:11]
	global_load_dword v93, v3, s[10:11] offset:1600
	global_load_dword v94, v3, s[10:11] offset:3200
	global_load_dword v95, v4, s[10:11]
	global_load_dword v96, v4, s[10:11] offset:1600
	global_load_dword v97, v4, s[10:11] offset:3200
	global_load_dword v98, v5, s[10:11]
	global_load_dword v99, v5, s[10:11] offset:1600
	s_nop 1
	v_mfma_f32_16x16x32_f16 a[0:3], v[10:13], v[14:17], a[0:3]
	s_waitcnt vmcnt(50)
	v_cvt_pk_f16_f32 v20, v108, v109
	v_cvt_pk_f16_f32 v21, v110, v111
	v_cvt_pk_f16_f32 v22, v112, v113
	v_cvt_pk_f16_f32 v23, v114, v115
	v_cvt_pk_f16_f32 v24, v116, v117
	v_cvt_pk_f16_f32 v25, v118, v119
	v_cvt_pk_f16_f32 v26, v120, v121
	v_cvt_pk_f16_f32 v27, v122, v123
	v_add_u32_e32 v3, 0x89800, v2
	v_add_u32_e32 v4, 0x8aac0, v2
	v_add_u32_e32 v5, 0x8bd80, v2
	global_load_dwordx4 v[116:119], v1, s[10:11] offset:1408
	global_load_dwordx4 v[120:123], v1, s[10:11] offset:1424
	global_load_dword v108, v3, s[10:11]
	global_load_dword v109, v3, s[10:11] offset:1600
	global_load_dword v110, v3, s[10:11] offset:3200
	global_load_dword v111, v4, s[10:11]
	global_load_dword v112, v4, s[10:11] offset:1600
	global_load_dword v113, v4, s[10:11] offset:3200
	global_load_dword v114, v5, s[10:11]
	global_load_dword v115, v5, s[10:11] offset:1600
	s_nop 1
	v_mfma_f32_16x16x32_f16 a[0:3], v[20:23], v[24:27], a[0:3]
	s_waitcnt vmcnt(50)
	v_cvt_pk_f16_f32 v10, v28, v29
	v_cvt_pk_f16_f32 v11, v30, v31
	v_cvt_pk_f16_f32 v12, v32, v33
	v_cvt_pk_f16_f32 v13, v34, v35
	v_cvt_pk_f16_f32 v14, v36, v37
	v_cvt_pk_f16_f32 v15, v38, v39
	v_cvt_pk_f16_f32 v16, v40, v41
	v_cvt_pk_f16_f32 v17, v42, v43
	v_mov_b32_e32 v28, 0
	v_mov_b32_e32 v29, 0
	v_mov_b32_e32 v30, 0
	v_mov_b32_e32 v31, 0
	v_mov_b32_e32 v32, 0
	v_mov_b32_e32 v33, 0
	v_mov_b32_e32 v34, 0
	v_mov_b32_e32 v35, 0
	v_mov_b32_e32 v36, 0
	v_mov_b32_e32 v37, 0
	v_mov_b32_e32 v38, 0
	v_mov_b32_e32 v39, 0
	v_mov_b32_e32 v40, 0
	v_mov_b32_e32 v41, 0
	v_mov_b32_e32 v42, 0
	v_mov_b32_e32 v43, 0
	v_cmp_gt_u32_e32 vcc, 2, v9
	s_and_saveexec_b64 s[4:5], vcc
	v_add_u32_e32 v3, 0x96000, v2
	v_add_u32_e32 v4, 0x972c0, v2
	v_add_u32_e32 v5, 0x98580, v2
	global_load_dwordx4 v[36:39], v1, s[10:11] offset:1536
	global_load_dwordx4 v[40:43], v1, s[10:11] offset:1552
	global_load_dword v28, v3, s[10:11]
	global_load_dword v29, v3, s[10:11] offset:1600
	global_load_dword v30, v3, s[10:11] offset:3200
	global_load_dword v31, v4, s[10:11]
	global_load_dword v32, v4, s[10:11] offset:1600
	global_load_dword v33, v4, s[10:11] offset:3200
	global_load_dword v34, v5, s[10:11]
	global_load_dword v35, v5, s[10:11] offset:1600
	s_mov_b64 exec, s[4:5]
	s_nop 1
	v_mfma_f32_16x16x32_f16 a[0:3], v[10:13], v[14:17], a[0:3]
	s_waitcnt vmcnt(50)
	v_cvt_pk_f16_f32 v20, v44, v45
	v_cvt_pk_f16_f32 v21, v46, v47
	v_cvt_pk_f16_f32 v22, v48, v49
	v_cvt_pk_f16_f32 v23, v50, v51
	v_cvt_pk_f16_f32 v24, v52, v53
	v_cvt_pk_f16_f32 v25, v54, v55
	v_cvt_pk_f16_f32 v26, v56, v57
	v_cvt_pk_f16_f32 v27, v58, v59
	s_nop 1
	v_mfma_f32_16x16x32_f16 a[0:3], v[20:23], v[24:27], a[0:3]
	s_waitcnt vmcnt(40)
	v_cvt_pk_f16_f32 v10, v60, v61
	v_cvt_pk_f16_f32 v11, v62, v63
	v_cvt_pk_f16_f32 v12, v64, v65
	v_cvt_pk_f16_f32 v13, v66, v67
	v_cvt_pk_f16_f32 v14, v68, v69
	v_cvt_pk_f16_f32 v15, v70, v71
	v_cvt_pk_f16_f32 v16, v72, v73
	v_cvt_pk_f16_f32 v17, v74, v75
	s_nop 1
	v_mfma_f32_16x16x32_f16 a[0:3], v[10:13], v[14:17], a[0:3]
	s_waitcnt vmcnt(30)
	v_cvt_pk_f16_f32 v20, v76, v77
	v_cvt_pk_f16_f32 v21, v78, v79
	v_cvt_pk_f16_f32 v22, v80, v81
	v_cvt_pk_f16_f32 v23, v82, v83
	v_cvt_pk_f16_f32 v24, v84, v85
	v_cvt_pk_f16_f32 v25, v86, v87
	v_cvt_pk_f16_f32 v26, v88, v89
	v_cvt_pk_f16_f32 v27, v90, v91
	s_nop 1
	v_mfma_f32_16x16x32_f16 a[0:3], v[20:23], v[24:27], a[0:3]
	s_waitcnt vmcnt(20)
	v_cvt_pk_f16_f32 v10, v92, v93
	v_cvt_pk_f16_f32 v11, v94, v95
	v_cvt_pk_f16_f32 v12, v96, v97
	v_cvt_pk_f16_f32 v13, v98, v99
	v_cvt_pk_f16_f32 v14, v100, v101
	v_cvt_pk_f16_f32 v15, v102, v103
	v_cvt_pk_f16_f32 v16, v104, v105
	v_cvt_pk_f16_f32 v17, v106, v107
	s_nop 1
	v_mfma_f32_16x16x32_f16 a[0:3], v[10:13], v[14:17], a[0:3]
	s_waitcnt vmcnt(10)
	v_cvt_pk_f16_f32 v20, v108, v109
	v_cvt_pk_f16_f32 v21, v110, v111
	v_cvt_pk_f16_f32 v22, v112, v113
	v_cvt_pk_f16_f32 v23, v114, v115
	v_cvt_pk_f16_f32 v24, v116, v117
	v_cvt_pk_f16_f32 v25, v118, v119
	v_cvt_pk_f16_f32 v26, v120, v121
	v_cvt_pk_f16_f32 v27, v122, v123
	s_nop 1
	v_mfma_f32_16x16x32_f16 a[0:3], v[20:23], v[24:27], a[0:3]
	s_waitcnt vmcnt(0)
	v_cvt_pk_f16_f32 v10, v28, v29
	v_cvt_pk_f16_f32 v11, v30, v31
	v_cvt_pk_f16_f32 v12, v32, v33
	v_cvt_pk_f16_f32 v13, v34, v35
	v_cvt_pk_f16_f32 v14, v36, v37
	v_cvt_pk_f16_f32 v15, v38, v39
	v_cvt_pk_f16_f32 v16, v40, v41
	v_cvt_pk_f16_f32 v17, v42, v43
	s_nop 1
	v_mfma_f32_16x16x32_f16 a[0:3], v[10:13], v[14:17], a[0:3]
	v_lshlrev_b32_e32 v10, 1, v8
	v_lshrrev_b32_e32 v1, 1, v9
	v_lshrrev_b32_e32 v2, 1, v8
	v_and_or_b32 v1, v10, 2, v1
	v_lshlrev_b32_e32 v3, 3, v7
	v_mad_u32_u24 v2, v6, 26, v2
	v_lshl_or_b32 v1, v1, 7, v3
	v_lshl_or_b32 v1, v2, 9, v1
	v_add_u32_e32 v18, 0x1a00, v1
	v_lshlrev_b32_e32 v2, 3, v9
	v_lshl_add_u64 v[4:5], v[18:19], 1, s[8:9]
	v_and_b32_e32 v18, 8, v2
	s_nop 7
	v_accvgpr_read_b32 v10, a0
	v_accvgpr_read_b32 v11, a1
	v_accvgpr_read_b32 v12, a2
	v_accvgpr_read_b32 v13, a3
	v_lshl_add_u64 v[4:5], v[4:5], 0, v[18:19]
	v_cvt_pk_f16_f32 v3, v12, v13
	v_cvt_pk_f16_f32 v2, v10, v11
	global_store_dwordx2 v[4:5], v[2:3], off

	.amdhsa_kernel _Z6k_prepPKf5WPtrsPDF16_S2_PfS3_P15HIP_vector_typeIjLj4EEi
		.amdhsa_group_segment_fixed_size 0
		.amdhsa_private_segment_fixed_size 0
		.amdhsa_kernarg_size 116
		.amdhsa_user_sgpr_count 2
		.amdhsa_user_sgpr_dispatch_ptr 0
		.amdhsa_user_sgpr_queue_ptr 0
		.amdhsa_user_sgpr_kernarg_segment_ptr 1
		.amdhsa_user_sgpr_dispatch_id 0
		.amdhsa_user_sgpr_kernarg_preload_length 0
		.amdhsa_user_sgpr_kernarg_preload_offset 0
		.amdhsa_user_sgpr_private_segment_size 0
		.amdhsa_uses_dynamic_stack 0
		.amdhsa_enable_private_segment 0
		.amdhsa_system_sgpr_workgroup_id_x 1
		.amdhsa_system_sgpr_workgroup_id_y 0
		.amdhsa_system_sgpr_workgroup_id_z 0
		.amdhsa_system_sgpr_workgroup_info 0
		.amdhsa_system_vgpr_workitem_id 0
		.amdhsa_next_free_vgpr 128
		.amdhsa_next_free_sgpr 48
		.amdhsa_accum_offset 124
		.amdhsa_reserve_vcc 1
		.amdhsa_float_round_mode_32 0
		.amdhsa_float_round_mode_16_64 0
		.amdhsa_float_denorm_mode_32 3
		.amdhsa_float_denorm_mode_16_64 3
		.amdhsa_dx10_clamp 1
		.amdhsa_ieee_mode 1
		.amdhsa_fp16_overflow 0
		.amdhsa_tg_split 0
		.amdhsa_exception_fp_ieee_invalid_op 0
		.amdhsa_exception_fp_denorm_src 0
		.amdhsa_exception_fp_ieee_div_zero 0
		.amdhsa_exception_fp_ieee_overflow 0
		.amdhsa_exception_fp_ieee_underflow 0
		.amdhsa_exception_fp_ieee_inexact 0
		.amdhsa_exception_int_div_zero 0
	.end_amdhsa_kernel

amdhsa.kernels:
  - .agpr_count:     4
    .args:
      - .actual_access:  read_only
        .address_space:  global
        .offset:         0
        .size:           8
        .value_kind:     global_buffer
      - .offset:         8
        .size:           64
        .value_kind:     by_value
      - .actual_access:  write_only
        .address_space:  global
        .offset:         72
        .size:           8
        .value_kind:     global_buffer
      - .actual_access:  write_only
        .address_space:  global
        .offset:         80
        .size:           8
        .value_kind:     global_buffer
      - .actual_access:  write_only
        .address_space:  global
        .offset:         88
        .size:           8
        .value_kind:     global_buffer
      - .actual_access:  write_only
        .address_space:  global
        .offset:         96
        .size:           8
        .value_kind:     global_buffer
      - .actual_access:  write_only
        .address_space:  global
        .offset:         104
        .size:           8
        .value_kind:     global_buffer
      - .offset:         112
        .size:           4
        .value_kind:     by_value
    .group_segment_fixed_size: 0
    .kernarg_segment_align: 8
    .kernarg_segment_size: 116
    .language:       OpenCL C
    .language_version:
      - 2
      - 0
    .max_flat_workgroup_size: 256
    .name:           _Z6k_prepPKf5WPtrsPDF16_S2_PfS3_P15HIP_vector_typeIjLj4EEi
    .private_segment_fixed_size: 0
    .sgpr_count:     54
    .sgpr_spill_count: 0
    .symbol:         _Z6k_prepPKf5WPtrsPDF16_S2_PfS3_P15HIP_vector_typeIjLj4EEi.kd
    .uniform_work_group_size: 1
    .uses_dynamic_stack: false
    .vgpr_count:     128
    .vgpr_spill_count: 0
    .wavefront_size: 64
  - .agpr_count:     241
    .args:
      - .offset:         0
        .size:           144
        .value_kind:     by_value
    .group_segment_fixed_size: 162192
    .kernarg_segment_align: 8
    .kernarg_segment_size: 144
    .language:       OpenCL C
    .language_version:
      - 2
      - 0
    .max_flat_workgroup_size: 256
    .name:           _Z9k_persist2PP
    .private_segment_fixed_size: 0
    .sgpr_count:     69
    .sgpr_spill_count: 0
    .symbol:         _Z9k_persist2PP.kd
    .uniform_work_group_size: 1
    .uses_dynamic_stack: false
    .vgpr_count:     497
    .vgpr_spill_count: 0
    .wavefront_size: 64
